# P6-idle CUs host conversion items [24576,39168) with two tiles in flight per wave; P4 converts [0,24576); nt loads on read-once f32 conversion inputs
# speedup vs baseline: 1.0157x; 1.0080x over previous
; #define LAS __attribute__((address_space(3)))
; #define LAS __attribute__((address_space(3)))
;     LAS unsigned* scr = (LAS unsigned*)(lds + wave * 16384);
;     WItem d0, d1; WRegs R0, R1;
;     constexpr int KB_ = DM / 32;
;     constexpr int NALL = EARLY ? KB_ * (INW / 128) : KB_ * (DM / 128) + KB_ * (CW / 128) + KB_ * (2 * CW / 128) + (CW / 32) * (DM / 128) + KB_ * (DFF2 / 128) + (DFF / 32) * (DM / 128);
;     const int hi_all = it_hi < NALL ? it_hi : NALL, total = hi_all - it_lo, nwgs = NGW / NWAVES, chunk = (((total + nwgs - 1) / nwgs) + NWAVES - 1) / NWAVES * NWAVES;
;     int it = it_lo + (gw / NWAVES) * chunk + (gw % NWAVES); const int wend0 = it_lo + (gw / NWAVES + 1) * chunk, wend = wend0 < hi_all ? wend0 : hi_all;
; __global__ void __launch_bounds__(NWAVES * 64, 2) mk_fwd(Args args) {
;     ...
;         const int NCONV = (CONV_OVERLAP && G >= 128) ? 51 : 0;
;         if (bx < NCONV) convert_weights<false, true>(P, lds, bx * NWAVES + wave, NCONV * NWAVES, wave, lane, 0, (CONV_OVERLAP && G >= 192) ? LATE_SPLIT : 0x7fffffff);
;         else {
;             sb_phase(lds, PROJ, (bf16*)(ws + WS_MIX), (const float*)(ws + WS_RSB), P.sbo_norm, bx - NCONV, G - NCONV, tid);
;             ret_out_phase(lds, PROJ, (bf16*)(ws + WS_MIX), (const bf16*)(ws + WS_ST), P.ret_norm, bx - NCONV, G - NCONV, tid);
;         }
;         if (NCONV == 0) convert_weights<false>(P, lds, gw, NGW, wave, lane);
.LBB0_519:
	s_mov_b32 s98, 0
	s_mov_b32 s99, 0
	s_mov_b32 s100, s80
	s_mov_b32 s101, s56
	s_mov_b32 s0, 0x9900
	s_cmp_eq_u32 s80, 0x100
	s_cselect_b32 s1, 1, 0
	s_cmp_gt_i32 s75, 6
	s_cselect_b32 s1, s1, 0
	s_cmp_lg_u32 s1, 0
	s_cselect_b32 s0, 0x6000, s0
	v_writelane_b32 v255, s0, 2
	s_mov_b32 s0, 0
	v_writelane_b32 v255, s0, 3

; #define GAS __attribute__((address_space(1)))
; template <bool UNCOND> DI void witem_load(const WItem& d, WRegs& R, int lane) {
;     const int n4 = lane & 31, kh = lane >> 5;
;     const float* src = d.W + (size_t)(d.k0 + 2 * kh) * d.N + d.src_col0 + 4 * n4;
; #pragma unroll
;     for (int i = 0; i < 8; ++i) { R.a[i] = *(const GAS f32x4*)(src + (size_t)(4 * i) * d.N); R.b[i] = *(const GAS f32x4*)(src + (size_t)(4 * i + 1) * d.N); }
;     if (UNCOND) {
;         const float* gp = d.gain ? d.gain + d.k0 + 2 * kh : src;
; #pragma unroll
;         for (int i = 0; i < 8; ++i) R.gg[i] = *(const GAS f32x2g*)(gp + 4 * i);
;         if (!d.gain) {
; #pragma unroll
;             for (int i = 0; i < 8; ++i) R.gg[i] = (f32x2g){1.f, 1.f}; }
;     } else if (d.gain) {
; #pragma unroll
;         for (int i = 0; i < 8; ++i) R.gg[i] = *(const GAS f32x2g*)(d.gain + d.k0 + 4 * i + 2 * kh); }
;     else {
; #pragma unroll
;         for (int i = 0; i < 8; ++i) R.gg[i] = (f32x2g){1.f, 1.f}; }
;     ...
;         const bool v1 = it + ST < wend && witem_decode<EARLY>(P, it + ST, d1);
;         if (PIPE) { if (!v1) d1 = d0; witem_load<true>(d1, R1, lane); } else if (v1) witem_load<false>(d1, R1, lane);
.LBB0_611:
	v_cndmask_b32_e64 v150, 0, 1, s[4:5]
	v_cmp_ne_u32_e64 s[0:1], 1, v150
	s_andn2_b64 vcc, exec, s[4:5]
	s_mov_b32 s100, 0
	s_cbranch_vccnz .LBB0_615
	v_add_u32_e32 v66, s36, v146
	v_mad_i64_i32 v[66:67], s[4:5], s38, v66, 0
	v_lshl_add_u64 v[66:67], v[66:67], 2, s[30:31]
	s_ashr_i32 s43, s42, 31
	s_ashr_i32 s39, s38, 31
	v_lshl_add_u64 v[66:67], s[42:43], 2, v[66:67]
	v_lshlrev_b32_e32 v150, 2, v148
	v_lshl_add_u64 v[66:67], v[66:67], 0, v[150:151]
	s_lshl_b64 s[4:5], s[38:39], 2
	v_lshl_add_u64 v[70:71], v[66:67], 0, s[4:5]
	global_load_dwordx4 v[66:69], v[66:67], off nt
	s_nop 0
	global_load_dwordx4 v[74:77], v[70:71], off nt
	v_mad_i64_i32 v[70:71], s[6:7], s38, 12, v[70:71]
	v_lshl_add_u64 v[78:79], v[70:71], 0, s[4:5]
	global_load_dwordx4 v[70:73], v[70:71], off nt
	s_nop 0
	global_load_dwordx4 v[82:85], v[78:79], off nt
	v_mad_i64_i32 v[78:79], s[6:7], s38, 12, v[78:79]
	v_lshl_add_u64 v[86:87], v[78:79], 0, s[4:5]
	global_load_dwordx4 v[78:81], v[78:79], off nt
	s_nop 0
	global_load_dwordx4 v[90:93], v[86:87], off nt
	v_mad_i64_i32 v[86:87], s[6:7], s38, 12, v[86:87]
	v_lshl_add_u64 v[94:95], v[86:87], 0, s[4:5]
	v_mad_i64_i32 v[102:103], s[6:7], s38, 12, v[94:95]
	global_load_dwordx4 v[86:89], v[86:87], off nt
	s_nop 0
	global_load_dwordx4 v[98:101], v[94:95], off nt
	s_cmp_eq_u64 s[34:35], 0
	global_load_dwordx4 v[94:97], v[102:103], off nt
	v_lshl_add_u64 v[102:103], v[102:103], 0, s[4:5]
	v_mad_i64_i32 v[110:111], s[6:7], s38, 12, v[102:103]
	global_load_dwordx4 v[106:109], v[102:103], off nt
	s_nop 0
	global_load_dwordx4 v[102:105], v[110:111], off nt
	v_lshl_add_u64 v[110:111], v[110:111], 0, s[4:5]
	v_mad_i64_i32 v[118:119], s[6:7], s38, 12, v[110:111]
	global_load_dwordx4 v[114:117], v[110:111], off nt
	s_nop 0
	global_load_dwordx4 v[110:113], v[118:119], off nt
	v_lshl_add_u64 v[118:119], v[118:119], 0, s[4:5]
	v_mad_i64_i32 v[126:127], s[6:7], s38, 12, v[118:119]
	global_load_dwordx4 v[122:125], v[118:119], off nt
	s_nop 0
	global_load_dwordx4 v[118:121], v[126:127], off nt
	v_lshl_add_u64 v[126:127], v[126:127], 0, s[4:5]
	global_load_dwordx4 v[126:129], v[126:127], off nt
	s_cbranch_scc1 .LBB0_614
	s_ashr_i32 s37, s36, 31
	s_lshl_b64 s[4:5], s[36:37], 2
	s_add_u32 s4, s34, s4
	s_addc_u32 s5, s35, s5
	v_lshlrev_b32_e32 v150, 2, v146
	s_mul_i32 s100, s98, 24
	global_load_dwordx2 v[152:153], v150, s[4:5]
	global_load_dwordx2 v[154:155], v150, s[4:5] offset:16
	global_load_dwordx2 v[156:157], v150, s[4:5] offset:32
	global_load_dwordx2 v[158:159], v150, s[4:5] offset:48
	global_load_dwordx2 v[160:161], v150, s[4:5] offset:64
	global_load_dwordx2 v[162:163], v150, s[4:5] offset:80
	global_load_dwordx2 v[164:165], v150, s[4:5] offset:96
	global_load_dwordx2 v[166:167], v150, s[4:5] offset:112
	s_branch .LBB0_615

; #define GAS __attribute__((address_space(1)))
; template <bool UNCOND> DI void witem_load(const WItem& d, WRegs& R, int lane) {
;     const int n4 = lane & 31, kh = lane >> 5;
;     const float* src = d.W + (size_t)(d.k0 + 2 * kh) * d.N + d.src_col0 + 4 * n4;
; #pragma unroll
;     for (int i = 0; i < 8; ++i) { R.a[i] = *(const GAS f32x4*)(src + (size_t)(4 * i) * d.N); R.b[i] = *(const GAS f32x4*)(src + (size_t)(4 * i + 1) * d.N); }
;     if (UNCOND) {
;         const float* gp = d.gain ? d.gain + d.k0 + 2 * kh : src;
; #pragma unroll
;         for (int i = 0; i < 8; ++i) R.gg[i] = *(const GAS f32x2g*)(gp + 4 * i);
;         if (!d.gain) {
; #pragma unroll
;             for (int i = 0; i < 8; ++i) R.gg[i] = (f32x2g){1.f, 1.f}; }
;     } else if (d.gain) {
; #pragma unroll
;         for (int i = 0; i < 8; ++i) R.gg[i] = *(const GAS f32x2g*)(d.gain + d.k0 + 4 * i + 2 * kh); }
;     else {
; #pragma unroll
;         for (int i = 0; i < 8; ++i) R.gg[i] = (f32x2g){1.f, 1.f}; }
;     ...
;         v0 = it + 2 * ST < wend && witem_decode<EARLY>(P, it + 2 * ST, d0);
;         if (PIPE) { if (!v0) d0 = d1; witem_load<true>(d0, R0, lane); } else if (v0) witem_load<false>(d0, R0, lane);
.LBB0_679:
	s_andn2_b64 vcc, exec, s[0:1]
	s_mov_b32 s100, 0
	s_cbranch_vccnz .LBB0_683
	v_add_u32_e32 v2, s14, v146
	v_mad_i64_i32 v[2:3], s[0:1], s16, v2, 0
	v_lshl_add_u64 v[2:3], v[2:3], 2, s[8:9]
	s_ashr_i32 s19, s18, 31
	s_ashr_i32 s17, s16, 31
	v_lshl_add_u64 v[2:3], s[18:19], 2, v[2:3]
	v_lshlrev_b32_e32 v150, 2, v148
	v_lshl_add_u64 v[2:3], v[2:3], 0, v[150:151]
	s_lshl_b64 s[0:1], s[16:17], 2
	v_lshl_add_u64 v[10:11], v[2:3], 0, s[0:1]
	global_load_dwordx4 v[6:9], v[2:3], off nt
	s_nop 0
	global_load_dwordx4 v[2:5], v[10:11], off nt
	v_mad_i64_i32 v[10:11], s[4:5], s16, 12, v[10:11]
	v_lshl_add_u64 v[18:19], v[10:11], 0, s[0:1]
	global_load_dwordx4 v[14:17], v[10:11], off nt
	s_nop 0
	global_load_dwordx4 v[10:13], v[18:19], off nt
	v_mad_i64_i32 v[18:19], s[4:5], s16, 12, v[18:19]
	v_lshl_add_u64 v[26:27], v[18:19], 0, s[0:1]
	global_load_dwordx4 v[22:25], v[18:19], off nt
	s_nop 0
	global_load_dwordx4 v[18:21], v[26:27], off nt
	v_mad_i64_i32 v[26:27], s[4:5], s16, 12, v[26:27]
	v_lshl_add_u64 v[34:35], v[26:27], 0, s[0:1]
	global_load_dwordx4 v[30:33], v[26:27], off nt
	s_nop 0
	global_load_dwordx4 v[26:29], v[34:35], off nt
	v_mad_i64_i32 v[34:35], s[4:5], s16, 12, v[34:35]
	v_lshl_add_u64 v[42:43], v[34:35], 0, s[0:1]
	global_load_dwordx4 v[38:41], v[34:35], off nt
	s_cmp_eq_u64 s[10:11], 0
	global_load_dwordx4 v[34:37], v[42:43], off nt
	v_mad_i64_i32 v[42:43], s[4:5], s16, 12, v[42:43]
	v_lshl_add_u64 v[50:51], v[42:43], 0, s[0:1]
	global_load_dwordx4 v[46:49], v[42:43], off nt
	s_nop 0
	global_load_dwordx4 v[42:45], v[50:51], off nt
	v_mad_i64_i32 v[50:51], s[4:5], s16, 12, v[50:51]
	v_lshl_add_u64 v[58:59], v[50:51], 0, s[0:1]
	global_load_dwordx4 v[54:57], v[50:51], off nt
	s_nop 0
	global_load_dwordx4 v[50:53], v[58:59], off nt
	v_mad_i64_i32 v[58:59], s[4:5], s16, 12, v[58:59]
	global_load_dwordx4 v[62:65], v[58:59], off nt
	v_lshl_add_u64 v[58:59], v[58:59], 0, s[0:1]
	global_load_dwordx4 v[58:61], v[58:59], off nt
	s_cbranch_scc1 .LBB0_682
	s_ashr_i32 s15, s14, 31
	s_lshl_b64 s[0:1], s[14:15], 2
	s_add_u32 s0, s10, s0
	s_addc_u32 s1, s11, s1
	v_lshlrev_b32_e32 v144, 2, v146
	s_mul_i32 s100, s98, 24
	global_load_dwordx2 v[130:131], v144, s[0:1]
	global_load_dwordx2 v[132:133], v144, s[0:1] offset:16
	global_load_dwordx2 v[134:135], v144, s[0:1] offset:32
	global_load_dwordx2 v[136:137], v144, s[0:1] offset:48
	global_load_dwordx2 v[138:139], v144, s[0:1] offset:64
	global_load_dwordx2 v[140:141], v144, s[0:1] offset:80
	global_load_dwordx2 v[142:143], v144, s[0:1] offset:96
	s_nop 0
	global_load_dwordx2 v[144:145], v144, s[0:1] offset:112
	s_branch .LBB0_683

;     ...
;     constexpr int NALL = EARLY ? KB_ * (INW / 128) : KB_ * (DM / 128) + KB_ * (CW / 128) + KB_ * (2 * CW / 128) + (CW / 32) * (DM / 128) + KB_ * (DFF2 / 128) + (DFF / 32) * (DM / 128);
;     const int hi_all = it_hi < NALL ? it_hi : NALL, total = hi_all - it_lo, nwgs = NGW / NWAVES, chunk = (((total + nwgs - 1) / nwgs) + NWAVES - 1) / NWAVES * NWAVES;
;     int it = it_lo + (gw / NWAVES) * chunk + (gw % NWAVES); const int wend0 = it_lo + (gw / NWAVES + 1) * chunk, wend = wend0 < hi_all ? wend0 : hi_all;
; __global__ void __launch_bounds__(NWAVES * 64, 2) mk_fwd(Args args) {
;     ...
;         if (CONV_OVERLAP && G >= 192 && bx >= G / 2 + 8) { __syncthreads(); convert_weights<false, true>(P, lds, (bx - (G / 2 + 8)) * NWAVES + wave, (G - (G / 2 + 8)) * NWAVES, wave, lane, LATE_SPLIT, 0x7fffffff); }
.LBB0_925:
	s_cmpk_lt_i32 s2, 0x88
	s_cbranch_scc1 .Lp6_hook_done
	s_cmp_lg_u32 s80, 0x100
	s_cbranch_scc1 .Lp6_hook_done
	s_cmp_gt_i32 s74, 4
	s_cbranch_scc1 .Lp6_hook_done
	s_cmp_lt_i32 s75, 7
	s_cbranch_scc1 .Lp6_hook_done
	v_writelane_b32 v255, s8, 8
	v_writelane_b32 v255, s9, 9
	v_writelane_b32 v255, s12, 10
	v_writelane_b32 v255, s16, 11
	v_writelane_b32 v255, s18, 12
	v_writelane_b32 v255, s19, 13
	v_writelane_b32 v255, s20, 14
	v_writelane_b32 v255, s21, 15
	v_writelane_b32 v255, s23, 16
	v_writelane_b32 v255, s24, 17
	v_writelane_b32 v255, s26, 18
	v_writelane_b32 v255, s34, 19
	v_readlane_b32 s70, v254, 0
	v_readlane_b32 s71, v254, 1
	v_and_b32_e32 v1, 63, v0
	v_readfirstlane_b32 s101, v0
	s_sub_u32 s100, s2, 0x88
	s_lshl_b32 s100, s100, 3
	s_sub_u32 s70, s70, 0xc0
	s_subb_u32 s71, s71, 0
	s_lshr_b32 s101, s101, 6
	s_add_u32 s101, s101, s100
	s_mov_b32 s100, 120
	s_mov_b32 s0, 0x3900
	v_writelane_b32 v255, s0, 2
	s_mov_b32 s0, 0x6000
	v_writelane_b32 v255, s0, 3
	s_mov_b32 s98, 1
	s_mov_b32 s99, 1
	s_mov_b64 s[4:5], -1
	s_branch .Lp4_conv_entry
